# window units: additionally skip P.V MFMAs and V tr-reads of tiles the wave found dead (on top of NA PV skip)
# speedup vs baseline: 1.0001x; 1.0001x over previous
.LBB0_640:
	s_add_i32 s26, s27, 2
	s_add_i32 s2, s5, s25
	s_addk_i32 s2, 0xff00
	s_add_i32 s3, s2, 0x5e
	s_sub_i32 s2, s2, 0x5e
	v_cmp_lt_i32_e32 vcc, s3, v175
	v_cmp_gt_i32_e64 s[2:3], s2, v176
	s_nop 1
	s_or_b64 s[2:3], vcc, s[2:3]
	s_cmp_ge_i32 s26, s20
	s_cselect_b64 s[2:3], 0, s[2:3]
	s_cmp_eq_u64 s[2:3], exec
	s_cbranch_scc1 .Lwin_deadA
	s_mov_b32 s100, 0
	ds_read_b128 v[64:67], v166 offset:49152
	ds_read_b128 v[230:233], v168 offset:49152
	ds_read_b128 v[234:237], v166 offset:57344
	ds_read_b128 v[238:241], v168 offset:57344
	v_add_f32_e32 v144, 0, v191
	v_add_f32_e32 v144, v201, v144
	v_add_f32_e32 v144, v145, v144
	v_add_f32_e32 v144, v200, v144
	v_add_f32_e32 v144, v146, v144
	v_add_f32_e32 v144, v190, v144
	v_add_f32_e32 v144, v147, v144
	v_add_f32_e32 v144, v189, v144
	v_add_f32_e32 v144, v186, v144
	v_add_f32_e32 v144, v188, v144
	v_add_f32_e32 v144, v185, v144
	v_add_f32_e32 v144, v187, v144
	v_exp_f32_e32 v142, v142
	v_add_f32_e32 v144, v182, v144
	v_exp_f32_e32 v143, v143
	v_add_f32_e32 v144, v184, v144
	v_exp_f32_e32 v140, v140
	v_add_f32_e32 v144, v181, v144
	v_exp_f32_e32 v141, v141
	v_add_f32_e32 v144, v183, v144
	v_exp_f32_e32 v138, v138
	v_add_f32_e32 v144, v142, v144
	v_exp_f32_e32 v139, v139
	v_add_f32_e32 v144, v143, v144
	v_exp_f32_e32 v136, v136
	v_add_f32_e32 v144, v140, v144
	v_exp_f32_e32 v137, v137
	v_add_f32_e32 v144, v141, v144
	v_exp_f32_e32 v134, v134
	v_add_f32_e32 v144, v138, v144
	v_exp_f32_e32 v135, v135
	v_add_f32_e32 v144, v139, v144
	v_exp_f32_e32 v132, v132
	v_add_f32_e32 v144, v136, v144
	v_exp_f32_e32 v133, v133
	v_add_f32_e32 v144, v137, v144
	v_exp_f32_e32 v130, v130
	v_add_f32_e32 v144, v134, v144
	v_exp_f32_e32 v131, v131
	v_add_f32_e32 v144, v135, v144
	v_exp_f32_e32 v128, v128
	v_add_f32_e32 v144, v132, v144
	v_exp_f32_e32 v129, v129
	v_add_f32_e32 v144, v133, v144
	v_add_f32_e32 v144, v130, v144
	v_add_f32_e32 v144, v131, v144
	v_add_f32_e32 v144, v128, v144
	v_add_f32_e32 v179, v129, v144
	v_mov_b32_e32 v180, v179
	v_cvt_pk_bf16_f32 v144, v191, v201
	v_cvt_pk_bf16_f32 v145, v145, v200
	v_cvt_pk_bf16_f32 v146, v146, v190
	v_cvt_pk_bf16_f32 v147, v147, v189
	v_cvt_pk_bf16_f32 v186, v186, v188
	v_cvt_pk_bf16_f32 v187, v185, v187
	v_cvt_pk_bf16_f32 v188, v182, v184
	v_cvt_pk_bf16_f32 v189, v181, v183
	v_cvt_pk_bf16_f32 v182, v142, v143
	v_cvt_pk_bf16_f32 v183, v140, v141
	v_cvt_pk_bf16_f32 v184, v138, v139
	v_cvt_pk_bf16_f32 v185, v136, v137
	v_cvt_pk_bf16_f32 v200, v134, v135
	v_cvt_pk_bf16_f32 v201, v132, v133
	v_cvt_pk_bf16_f32 v202, v130, v131
	s_nop 0
	v_permlane32_swap_b32_e32 v179, v180
	v_permlane32_swap_b32_e32 v144, v146
	v_cvt_pk_bf16_f32 v203, v128, v129
	v_permlane32_swap_b32_e32 v200, v202
	v_permlane32_swap_b32_e32 v145, v147
	v_permlane32_swap_b32_e32 v186, v188
	v_permlane32_swap_b32_e32 v187, v189
	v_permlane32_swap_b32_e32 v182, v184
	v_permlane32_swap_b32_e32 v183, v185
	v_permlane32_swap_b32_e32 v201, v203
	s_add_i32 s2, s27, 3
	s_cmp_lt_i32 s2, s20
	s_cselect_b64 s[8:9], -1, 0
	s_and_b64 s[2:3], s[8:9], exec
	s_cselect_b32 s2, 0, s20
	s_cselect_b32 s3, s19, 0x4000
	s_lshl_b32 s2, s2, 6
	s_sub_i32 s2, s3, s2
	s_add_i32 s2, s25, s2
	s_mulk_i32 s2, 0x2400
	s_add_i32 s10, s2, 0xfff70000
	s_add_u32 s2, s21, s10
	s_addc_u32 s3, s22, 0
	s_add_u32 s10, s23, s10
	s_addc_u32 s11, s24, 0
	v_lshl_add_u64 v[128:129], s[10:11], 0, v[192:193]
	v_lshl_add_u64 v[132:133], s[10:11], 0, v[152:153]
	v_lshl_add_u64 v[136:137], s[2:3], 0, v[192:193]
	v_lshl_add_u64 v[140:141], s[2:3], 0, v[152:153]
	global_load_dwordx4 v[128:131], v[128:129], off
	s_nop 0
	global_load_dwordx4 v[132:135], v[132:133], off
	s_nop 0
	global_load_dwordx4 v[136:139], v[136:137], off
	s_nop 0
	global_load_dwordx4 v[140:143], v[140:141], off
	s_cmp_ge_i32 s26, s20
	s_waitcnt lgkmcnt(3)
	v_mfma_f32_32x32x16_bf16 v[80:95], v[64:67], v[124:127], 0
	s_waitcnt lgkmcnt(2)
	v_mfma_f32_32x32x16_bf16 v[80:95], v[230:233], v[120:123], v[80:95]
	ds_read_b128 v[230:233], v167 offset:49152
	s_waitcnt lgkmcnt(2)
	v_mfma_f32_32x32x16_bf16 v[64:79], v[234:237], v[124:127], 0
	ds_read_b128 v[234:237], v167 offset:57344
	s_waitcnt lgkmcnt(2)
	v_mfma_f32_32x32x16_bf16 v[64:79], v[238:241], v[120:123], v[64:79]
	ds_read_b128 v[238:241], v165 offset:49152
	s_waitcnt lgkmcnt(2)
	v_mfma_f32_32x32x16_bf16 v[80:95], v[230:233], v[116:119], v[80:95]
	ds_read_b128 v[230:233], v165 offset:57344
	s_waitcnt lgkmcnt(2)
	v_mfma_f32_32x32x16_bf16 v[64:79], v[234:237], v[116:119], v[64:79]
	ds_read_b128 v[234:237], v164 offset:49152
	s_waitcnt lgkmcnt(2)
	v_mfma_f32_32x32x16_bf16 v[80:95], v[238:241], v[112:115], v[80:95]
	ds_read_b128 v[238:241], v164 offset:57344
	s_waitcnt lgkmcnt(2)
	v_mfma_f32_32x32x16_bf16 v[64:79], v[230:233], v[112:115], v[64:79]
	ds_read_b128 v[230:233], v163 offset:49152
	s_waitcnt lgkmcnt(2)
	v_mfma_f32_32x32x16_bf16 v[80:95], v[234:237], v[108:111], v[80:95]
	ds_read_b128 v[234:237], v163 offset:57344
	s_waitcnt lgkmcnt(2)
	v_mfma_f32_32x32x16_bf16 v[64:79], v[238:241], v[108:111], v[64:79]
	ds_read_b128 v[238:241], v162 offset:49152
	s_waitcnt lgkmcnt(2)
	v_mfma_f32_32x32x16_bf16 v[80:95], v[230:233], v[104:107], v[80:95]
	ds_read_b128 v[230:233], v162 offset:57344
	s_waitcnt lgkmcnt(2)
	v_mfma_f32_32x32x16_bf16 v[64:79], v[234:237], v[104:107], v[64:79]
	ds_read_b128 v[234:237], v161 offset:49152
	s_waitcnt lgkmcnt(2)
	v_mfma_f32_32x32x16_bf16 v[80:95], v[238:241], v[100:103], v[80:95]
	ds_read_b128 v[238:241], v161 offset:57344
	s_waitcnt lgkmcnt(2)
	v_mfma_f32_32x32x16_bf16 v[64:79], v[230:233], v[100:103], v[64:79]
	s_waitcnt lgkmcnt(1)
	v_mfma_f32_32x32x16_bf16 v[80:95], v[234:237], v[96:99], v[80:95]
	s_waitcnt lgkmcnt(0)
	v_mfma_f32_32x32x16_bf16 v[64:79], v[238:241], v[96:99], v[64:79]
	s_cbranch_scc1 .LBB0_644
	s_add_i32 s2, s5, s25
	s_addk_i32 s2, 0xff00
	v_cmp_lt_i32_e32 vcc, s2, v175
	v_cmp_gt_i32_e64 s[2:3], s2, v176
	s_or_b64 s[8:9], vcc, s[2:3]
	s_and_saveexec_b64 s[2:3], s[8:9]
	s_cbranch_execz .LBB0_643
	v_add_u32_e32 v242, s25, v178
	v_add_u32_e32 v243, 0xffffff80, v242
	s_movk_i32 s8, 0x101
	v_cmp_gt_u32_e32 vcc, s8, v243
	v_add_u32_e32 v243, 0xffffffa0, v242
	s_nop 0
	v_cndmask_b32_e32 v80, v217, v80, vcc
	v_cmp_gt_u32_e32 vcc, s8, v243
	v_add_u32_e32 v243, 0xffffff81, v242
	s_nop 0
	v_cndmask_b32_e32 v64, v217, v64, vcc
	v_cmp_gt_u32_e32 vcc, s8, v243
	v_add_u32_e32 v243, 0xffffffa1, v242
	s_nop 0
	v_cndmask_b32_e32 v81, v217, v81, vcc
	v_cmp_gt_u32_e32 vcc, s8, v243
	v_add_u32_e32 v243, 0xffffff82, v242
	s_nop 0
	v_cndmask_b32_e32 v65, v217, v65, vcc
	v_cmp_gt_u32_e32 vcc, s8, v243
	v_add_u32_e32 v243, 0xffffffa2, v242
	s_nop 0
	v_cndmask_b32_e32 v82, v217, v82, vcc
	v_cmp_gt_u32_e32 vcc, s8, v243
	v_add_u32_e32 v243, 0xffffff83, v242
	s_nop 0
	v_cndmask_b32_e32 v66, v217, v66, vcc
	v_cmp_gt_u32_e32 vcc, s8, v243
	v_add_u32_e32 v243, 0xffffffa3, v242
	s_nop 0
	v_cndmask_b32_e32 v83, v217, v83, vcc
	v_cmp_gt_u32_e32 vcc, s8, v243
	v_add_u32_e32 v243, 0xffffff88, v242
	s_nop 0
	v_cndmask_b32_e32 v67, v217, v67, vcc
	v_cmp_gt_u32_e32 vcc, s8, v243
	v_add_u32_e32 v243, 0xffffffa8, v242
	s_nop 0
	v_cndmask_b32_e32 v84, v217, v84, vcc
	v_cmp_gt_u32_e32 vcc, s8, v243
	v_add_u32_e32 v243, 0xffffff89, v242
	s_nop 0
	v_cndmask_b32_e32 v68, v217, v68, vcc
	v_cmp_gt_u32_e32 vcc, s8, v243
	v_add_u32_e32 v243, 0xffffffa9, v242
	s_nop 0
	v_cndmask_b32_e32 v85, v217, v85, vcc
	v_cmp_gt_u32_e32 vcc, s8, v243
	v_add_u32_e32 v243, 0xffffff8a, v242
	s_nop 0
	v_cndmask_b32_e32 v69, v217, v69, vcc
	v_cmp_gt_u32_e32 vcc, s8, v243
	v_add_u32_e32 v243, 0xffffffaa, v242
	s_nop 0
	v_cndmask_b32_e32 v86, v217, v86, vcc
	v_cmp_gt_u32_e32 vcc, s8, v243
	v_add_u32_e32 v243, 0xffffff8b, v242
	s_nop 0
	v_cndmask_b32_e32 v70, v217, v70, vcc
	v_cmp_gt_u32_e32 vcc, s8, v243
	v_add_u32_e32 v243, 0xffffffab, v242
	s_nop 0
	v_cndmask_b32_e32 v87, v217, v87, vcc
	v_cmp_gt_u32_e32 vcc, s8, v243
	v_add_u32_e32 v243, 0xffffff90, v242
	s_nop 0
	v_cndmask_b32_e32 v71, v217, v71, vcc
	v_cmp_gt_u32_e32 vcc, s8, v243
	v_add_u32_e32 v243, 0xffffffb0, v242
	s_nop 0
	v_cndmask_b32_e32 v88, v217, v88, vcc
	v_cmp_gt_u32_e32 vcc, s8, v243
	v_add_u32_e32 v243, 0xffffff91, v242
	s_nop 0
	v_cndmask_b32_e32 v72, v217, v72, vcc
	v_cmp_gt_u32_e32 vcc, s8, v243
	v_add_u32_e32 v243, 0xffffffb1, v242
	s_nop 0
	v_cndmask_b32_e32 v89, v217, v89, vcc
	v_cmp_gt_u32_e32 vcc, s8, v243
	v_add_u32_e32 v243, 0xffffff92, v242
	s_nop 0
	v_cndmask_b32_e32 v73, v217, v73, vcc
	v_cmp_gt_u32_e32 vcc, s8, v243
	v_add_u32_e32 v243, 0xffffffb2, v242
	s_nop 0
	v_cndmask_b32_e32 v90, v217, v90, vcc
	v_cmp_gt_u32_e32 vcc, s8, v243
	v_add_u32_e32 v243, 0xffffff93, v242
	s_nop 0
	v_cndmask_b32_e32 v74, v217, v74, vcc
	v_cmp_gt_u32_e32 vcc, s8, v243
	v_add_u32_e32 v243, 0xffffffb3, v242
	s_nop 0
	v_cndmask_b32_e32 v91, v217, v91, vcc
	v_cmp_gt_u32_e32 vcc, s8, v243
	v_add_u32_e32 v243, 0xffffff98, v242
	s_nop 0
	v_cndmask_b32_e32 v75, v217, v75, vcc
	v_cmp_gt_u32_e32 vcc, s8, v243
	v_add_u32_e32 v243, 0xffffffb8, v242
	s_nop 0
	v_cndmask_b32_e32 v92, v217, v92, vcc
	v_cmp_gt_u32_e32 vcc, s8, v243
	v_add_u32_e32 v243, 0xffffff99, v242
	s_nop 0
	v_cndmask_b32_e32 v76, v217, v76, vcc
	v_cmp_gt_u32_e32 vcc, s8, v243
	v_add_u32_e32 v243, 0xffffffb9, v242
	s_nop 0
	v_cndmask_b32_e32 v93, v217, v93, vcc
	v_cmp_gt_u32_e32 vcc, s8, v243
	v_add_u32_e32 v243, 0xffffff9a, v242
	s_nop 0
	v_cndmask_b32_e32 v77, v217, v77, vcc
	v_cmp_gt_u32_e32 vcc, s8, v243
	v_add_u32_e32 v243, 0xffffffba, v242
	s_nop 0
	v_cndmask_b32_e32 v94, v217, v94, vcc
	v_cmp_gt_u32_e32 vcc, s8, v243
	v_add_u32_e32 v243, 0xffffff9b, v242
	v_add_u32_e32 v242, 0xffffffbb, v242
	v_cndmask_b32_e32 v78, v217, v78, vcc
	v_cmp_gt_u32_e32 vcc, s8, v243
	s_nop 1
	v_cndmask_b32_e32 v95, v217, v95, vcc
	v_cmp_gt_u32_e32 vcc, s8, v242
	s_nop 1
	v_cndmask_b32_e32 v79, v217, v79, vcc

.LBB0_644:
	s_add_i32 s2, s27, 3
	s_cmp_lt_i32 s2, s20
	s_cselect_b64 s[8:9], -1, 0
	s_cmp_eq_u32 s101, 1
	s_cbranch_scc1 .Lwin_pvdB
	ds_read_b64_tr_b16 v[204:205], v160 offset:0
	ds_read_b64_tr_b16 v[206:207], v160 offset:0x800
	ds_read_b64_tr_b16 v[208:209], v160 offset:0x1000
	ds_read_b64_tr_b16 v[210:211], v160 offset:0x1800
	ds_read_b64_tr_b16 v[212:213], v160 offset:0x2000
	ds_read_b64_tr_b16 v[214:215], v160 offset:0x2800
	ds_read_b64_tr_b16 v[218:219], v160 offset:0x3000
	ds_read_b64_tr_b16 v[220:221], v160 offset:0x3800
	s_waitcnt lgkmcnt(0)
	s_nop 0
	v_mfma_f32_32x32x16_bf16 v[48:63], v[144:147], v[204:207], v[48:63]
	ds_read_b64_tr_b16 v[204:205], v160 offset:0x200
	ds_read_b64_tr_b16 v[206:207], v160 offset:0xa00
	v_mfma_f32_32x32x16_bf16 v[48:63], v[186:189], v[208:211], v[48:63]
	ds_read_b64_tr_b16 v[208:209], v160 offset:0x1200
	ds_read_b64_tr_b16 v[210:211], v160 offset:0x1a00
	v_mfma_f32_32x32x16_bf16 v[48:63], v[182:185], v[212:215], v[48:63]
	ds_read_b64_tr_b16 v[212:213], v160 offset:0x2200
	ds_read_b64_tr_b16 v[214:215], v160 offset:0x2a00
	v_mfma_f32_32x32x16_bf16 v[48:63], v[200:203], v[218:221], v[48:63]
	ds_read_b64_tr_b16 v[218:219], v160 offset:0x3200
	ds_read_b64_tr_b16 v[220:221], v160 offset:0x3a00
	s_waitcnt lgkmcnt(0)
	v_mfma_f32_32x32x16_bf16 v[32:47], v[144:147], v[204:207], v[32:47]
	ds_read_b64_tr_b16 v[204:205], v160 offset:0x400
	ds_read_b64_tr_b16 v[206:207], v160 offset:0xc00
	v_mfma_f32_32x32x16_bf16 v[32:47], v[186:189], v[208:211], v[32:47]
	ds_read_b64_tr_b16 v[208:209], v160 offset:0x1400
	ds_read_b64_tr_b16 v[210:211], v160 offset:0x1c00
	v_mfma_f32_32x32x16_bf16 v[32:47], v[182:185], v[212:215], v[32:47]
	ds_read_b64_tr_b16 v[212:213], v160 offset:0x2400
	ds_read_b64_tr_b16 v[214:215], v160 offset:0x2c00
	v_mfma_f32_32x32x16_bf16 v[32:47], v[200:203], v[218:221], v[32:47]
	ds_read_b64_tr_b16 v[218:219], v160 offset:0x3400
	ds_read_b64_tr_b16 v[220:221], v160 offset:0x3c00
	s_waitcnt lgkmcnt(0)
	v_mfma_f32_32x32x16_bf16 v[16:31], v[144:147], v[204:207], v[16:31]
	ds_read_b64_tr_b16 v[204:205], v160 offset:0x600
	ds_read_b64_tr_b16 v[206:207], v160 offset:0xe00
	v_mfma_f32_32x32x16_bf16 v[16:31], v[186:189], v[208:211], v[16:31]
	ds_read_b64_tr_b16 v[208:209], v160 offset:0x1600
	ds_read_b64_tr_b16 v[210:211], v160 offset:0x1e00
	v_mfma_f32_32x32x16_bf16 v[16:31], v[182:185], v[212:215], v[16:31]
	ds_read_b64_tr_b16 v[212:213], v160 offset:0x2600
	ds_read_b64_tr_b16 v[214:215], v160 offset:0x2e00
	v_mfma_f32_32x32x16_bf16 v[16:31], v[200:203], v[218:221], v[16:31]
	ds_read_b64_tr_b16 v[218:219], v160 offset:0x3600
	ds_read_b64_tr_b16 v[220:221], v160 offset:0x3e00
	s_waitcnt lgkmcnt(0)
	v_mfma_f32_32x32x16_bf16 v[0:15], v[144:147], v[204:207], v[0:15]
	v_max_f32_e32 v144, v81, v81
	v_max_f32_e32 v145, v80, v80
	v_max_f32_e32 v144, v145, v144
	v_max3_f32 v144, v144, v82, v83
	v_max3_f32 v144, v144, v84, v85
	v_max3_f32 v144, v144, v86, v87
	v_max3_f32 v144, v144, v88, v89
	v_max3_f32 v144, v144, v90, v91
	v_max3_f32 v144, v144, v92, v93
	v_mfma_f32_32x32x16_bf16 v[0:15], v[186:189], v[208:211], v[0:15]
	v_max3_f32 v144, v144, v94, v95
	v_max3_f32 v144, v144, v64, v65
	v_max3_f32 v144, v144, v66, v67
	v_max3_f32 v144, v144, v68, v69
	v_max3_f32 v144, v144, v70, v71
	v_max3_f32 v144, v144, v72, v73
	v_max3_f32 v144, v144, v74, v75
	v_max3_f32 v144, v144, v76, v77
	v_mfma_f32_32x32x16_bf16 v[0:15], v[182:185], v[212:215], v[0:15]
	v_max3_f32 v144, v144, v78, v79
	v_mov_b32_e32 v145, v144
	s_nop 1
	v_permlane32_swap_b32_e32 v144, v145
	v_max_f32_e32 v145, v145, v145
	v_max_f32_e32 v144, v144, v144
	v_max_f32_e32 v144, v144, v145
	v_sub_f32_e32 v145, v144, v174
	s_mov_b32 s2, 0x42b504f3
	v_cmp_ge_f32_e32 vcc, s2, v145
	v_max_f32_e32 v145, v174, v174
	v_max_f32_e32 v144, v145, v144
	v_mfma_f32_32x32x16_bf16 v[0:15], v[200:203], v[218:221], v[0:15]
	v_sub_f32_e32 v145, v174, v144
	v_mul_f32_e32 v145, 0x3e0293ee, v145
	v_exp_f32_e32 v145, v145
	s_cmp_eq_u64 vcc, exec
	s_cselect_b64 s[2:3], -1, 0
.Lwin_pvjB:
	s_barrier
	s_waitcnt vmcnt(0)
	v_cndmask_b32_e64 v202, v145, 1.0, s[2:3]
	v_cmp_gt_f32_e32 vcc, 1.0, v202
	s_waitcnt vmcnt(3)
	ds_write_b128 v169, v[128:131]
	s_waitcnt vmcnt(2)
	ds_write_b128 v170, v[132:135]
	s_waitcnt vmcnt(1)
	ds_write_b128 v171, v[136:139] offset:32768
	s_waitcnt vmcnt(0)
	ds_write_b128 v172, v[140:143] offset:32768
	s_cbranch_vccz .LBB0_648
	s_and_saveexec_b64 s[10:11], s[0:1]
	ds_write_b32 v158, v202 offset:128
	s_or_b64 exec, exec, s[10:11]
	s_waitcnt lgkmcnt(0)
	v_add_u32_e32 v140, v151, v150
	ds_read_b128 v[128:131], v140 offset:224
	ds_read_b128 v[132:135], v140 offset:192
	ds_read_b128 v[136:139], v140 offset:160
	ds_read_b128 v[140:143], v140 offset:128
	s_waitcnt lgkmcnt(3)
	v_pk_mul_f32 v[60:61], v[60:61], v[128:129]
	s_waitcnt lgkmcnt(2)
	v_pk_mul_f32 v[56:57], v[56:57], v[132:133]
	s_waitcnt lgkmcnt(1)
	v_pk_mul_f32 v[52:53], v[52:53], v[136:137]
	v_pk_mul_f32 v[62:63], v[62:63], v[130:131]
	v_pk_mul_f32 v[58:59], v[58:59], v[134:135]
	v_pk_mul_f32 v[54:55], v[54:55], v[138:139]
	s_waitcnt lgkmcnt(0)
	v_pk_mul_f32 v[50:51], v[50:51], v[142:143]
	v_pk_mul_f32 v[48:49], v[48:49], v[140:141]
	v_pk_mul_f32 v[44:45], v[44:45], v[128:129]
	v_pk_mul_f32 v[40:41], v[40:41], v[132:133]
	v_pk_mul_f32 v[36:37], v[36:37], v[136:137]
	v_pk_mul_f32 v[46:47], v[46:47], v[130:131]
	v_pk_mul_f32 v[42:43], v[42:43], v[134:135]
	v_pk_mul_f32 v[38:39], v[38:39], v[138:139]
	v_pk_mul_f32 v[34:35], v[34:35], v[142:143]
	v_pk_mul_f32 v[32:33], v[32:33], v[140:141]
	v_pk_mul_f32 v[28:29], v[28:29], v[128:129]
	v_pk_mul_f32 v[24:25], v[24:25], v[132:133]
	v_pk_mul_f32 v[20:21], v[20:21], v[136:137]
	v_pk_mul_f32 v[30:31], v[30:31], v[130:131]
	v_pk_mul_f32 v[26:27], v[26:27], v[134:135]
	v_pk_mul_f32 v[22:23], v[22:23], v[138:139]
	v_pk_mul_f32 v[18:19], v[18:19], v[142:143]
	v_pk_mul_f32 v[16:17], v[16:17], v[140:141]
	v_pk_mul_f32 v[12:13], v[12:13], v[128:129]
	v_pk_mul_f32 v[8:9], v[8:9], v[132:133]
	v_pk_mul_f32 v[4:5], v[4:5], v[136:137]
	v_pk_mul_f32 v[14:15], v[14:15], v[130:131]
	v_pk_mul_f32 v[10:11], v[10:11], v[134:135]
	v_pk_mul_f32 v[6:7], v[6:7], v[138:139]
	v_pk_mul_f32 v[2:3], v[2:3], v[142:143]
	v_pk_mul_f32 v[0:1], v[0:1], v[140:141]
.LBB0_648:
	v_cndmask_b32_e64 v174, v144, v174, s[2:3]
	v_mul_f32_e32 v144, 0xbe0293ee, v174
	v_fmamk_f32 v80, v80, 0x3e0293ee, v144
	v_fmamk_f32 v81, v81, 0x3e0293ee, v144
	v_fmamk_f32 v82, v82, 0x3e0293ee, v144
	v_fmamk_f32 v83, v83, 0x3e0293ee, v144
	v_fmamk_f32 v84, v84, 0x3e0293ee, v144
	v_fmamk_f32 v85, v85, 0x3e0293ee, v144
	v_fmamk_f32 v86, v86, 0x3e0293ee, v144
	v_fmamk_f32 v87, v87, 0x3e0293ee, v144
	v_fmamk_f32 v88, v88, 0x3e0293ee, v144
	v_fmamk_f32 v89, v89, 0x3e0293ee, v144
	v_fmamk_f32 v90, v90, 0x3e0293ee, v144
	v_fmamk_f32 v91, v91, 0x3e0293ee, v144
	v_fmamk_f32 v92, v92, 0x3e0293ee, v144
	v_fmamk_f32 v93, v93, 0x3e0293ee, v144
	v_fmamk_f32 v94, v94, 0x3e0293ee, v144
	v_fmamk_f32 v95, v95, 0x3e0293ee, v144
	v_exp_f32_e32 v141, v80
	v_exp_f32_e32 v143, v81
	v_exp_f32_e32 v139, v82
	v_exp_f32_e32 v142, v83
	v_exp_f32_e32 v137, v84
	v_exp_f32_e32 v140, v85
	v_exp_f32_e32 v136, v86
	v_exp_f32_e32 v138, v87
	v_exp_f32_e32 v133, v88
	v_exp_f32_e32 v135, v89
	v_exp_f32_e32 v131, v90
	v_exp_f32_e32 v134, v91
	v_exp_f32_e32 v129, v92
	v_exp_f32_e32 v132, v93
	v_exp_f32_e32 v128, v94
	v_exp_f32_e32 v130, v95
	v_fmamk_f32 v145, v64, 0x3e0293ee, v144
	v_fmamk_f32 v146, v65, 0x3e0293ee, v144
	v_fmamk_f32 v147, v66, 0x3e0293ee, v144
	v_fmamk_f32 v181, v67, 0x3e0293ee, v144
	v_fmamk_f32 v182, v68, 0x3e0293ee, v144
	v_fmamk_f32 v183, v69, 0x3e0293ee, v144
	v_fmamk_f32 v184, v70, 0x3e0293ee, v144
	v_fmamk_f32 v185, v71, 0x3e0293ee, v144
	v_fmamk_f32 v186, v72, 0x3e0293ee, v144
	v_fmamk_f32 v187, v73, 0x3e0293ee, v144
	v_fmamk_f32 v188, v74, 0x3e0293ee, v144
	v_fmamk_f32 v189, v75, 0x3e0293ee, v144
	v_fmamk_f32 v190, v76, 0x3e0293ee, v144
	v_fmamk_f32 v191, v77, 0x3e0293ee, v144
	v_fmamk_f32 v200, v78, 0x3e0293ee, v144
	v_fmac_f32_e32 v144, 0x3e0293ee, v79
	s_waitcnt lgkmcnt(0)
	s_barrier
	s_add_i32 s2, s5, s25
	s_addk_i32 s2, 0xff40
	s_add_i32 s3, s2, 0x5e
	s_sub_i32 s2, s2, 0x5e
	v_cmp_lt_i32_e32 vcc, s3, v175
	v_cmp_gt_i32_e64 s[2:3], s2, v176
	s_nop 1
	s_or_b64 s[2:3], vcc, s[2:3]
	s_and_b64 s[2:3], s[2:3], s[8:9]
	s_cmp_eq_u64 s[2:3], exec
	s_cbranch_scc1 .Lwin_deadB
	s_mov_b32 s101, 0
	ds_read_b128 v[64:67], v166 offset:32768
	ds_read_b128 v[230:233], v168 offset:32768
	ds_read_b128 v[234:237], v166 offset:40960
	ds_read_b128 v[238:241], v168 offset:40960
	s_andn2_b64 vcc, exec, s[8:9]
	v_exp_f32_e32 v215, v144
	v_add_f32_e32 v144, 0, v141
	v_add_f32_e32 v144, v143, v144
	v_add_f32_e32 v144, v139, v144
	v_add_f32_e32 v144, v142, v144
	v_add_f32_e32 v144, v137, v144
	v_add_f32_e32 v144, v140, v144
	v_add_f32_e32 v144, v136, v144
	v_add_f32_e32 v144, v138, v144
	v_add_f32_e32 v144, v133, v144
	v_add_f32_e32 v144, v135, v144
	v_add_f32_e32 v144, v131, v144
	v_add_f32_e32 v144, v134, v144
	v_exp_f32_e32 v201, v145
	v_add_f32_e32 v144, v129, v144
	v_exp_f32_e32 v205, v146
	v_add_f32_e32 v144, v132, v144
	v_exp_f32_e32 v206, v147
	v_add_f32_e32 v144, v128, v144
	v_exp_f32_e32 v181, v181
	v_add_f32_e32 v144, v130, v144
	v_exp_f32_e32 v207, v182
	v_add_f32_e32 v144, v201, v144
	v_exp_f32_e32 v208, v183
	v_add_f32_e32 v144, v205, v144
	v_exp_f32_e32 v209, v184
	v_add_f32_e32 v144, v206, v144
	v_exp_f32_e32 v210, v185
	v_add_f32_e32 v144, v181, v144
	v_exp_f32_e32 v211, v186
	v_add_f32_e32 v144, v207, v144
	v_exp_f32_e32 v212, v187
	v_add_f32_e32 v144, v208, v144
	v_exp_f32_e32 v213, v188
	v_add_f32_e32 v144, v209, v144
	v_exp_f32_e32 v214, v189
	v_add_f32_e32 v144, v210, v144
	v_exp_f32_e32 v190, v190
	v_add_f32_e32 v144, v211, v144
	v_exp_f32_e32 v191, v191
	v_add_f32_e32 v144, v212, v144
	v_exp_f32_e32 v200, v200
	v_add_f32_e32 v144, v213, v144
	v_add_f32_e32 v144, v214, v144
	v_add_f32_e32 v144, v190, v144
	v_add_f32_e32 v144, v191, v144
	v_add_f32_e32 v144, v200, v144
	v_add_f32_e32 v203, v215, v144
	v_mov_b32_e32 v204, v203
	v_cvt_pk_bf16_f32 v144, v141, v143
	v_cvt_pk_bf16_f32 v145, v139, v142
	v_cvt_pk_bf16_f32 v146, v137, v140
	v_cvt_pk_bf16_f32 v147, v136, v138
	s_nop 1
	v_permlane32_swap_b32_e32 v203, v204
	v_permlane32_swap_b32_e32 v144, v146
	v_permlane32_swap_b32_e32 v145, v147
	v_cvt_pk_bf16_f32 v182, v133, v135
	v_cvt_pk_bf16_f32 v183, v131, v134
	v_cvt_pk_bf16_f32 v184, v129, v132
	v_cvt_pk_bf16_f32 v185, v128, v130
	v_cvt_pk_bf16_f32 v186, v201, v205
	v_cvt_pk_bf16_f32 v187, v206, v181
	v_cvt_pk_bf16_f32 v188, v207, v208
	v_cvt_pk_bf16_f32 v189, v209, v210
	v_cvt_pk_bf16_f32 v206, v211, v212
	v_cvt_pk_bf16_f32 v207, v213, v214
	v_cvt_pk_bf16_f32 v208, v190, v191
	v_cvt_pk_bf16_f32 v209, v200, v215
	s_nop 0
	v_permlane32_swap_b32_e32 v182, v184
	v_permlane32_swap_b32_e32 v183, v185
	v_permlane32_swap_b32_e32 v186, v188
	v_permlane32_swap_b32_e32 v187, v189
	v_permlane32_swap_b32_e32 v206, v208
	v_permlane32_swap_b32_e32 v207, v209
	s_add_i32 s2, s27, 4
	s_cmp_lt_i32 s2, s20
	s_cselect_b32 s2, 0, s20
	s_cselect_b32 s3, s19, 0x4000
	s_lshl_b32 s2, s2, 6
	s_sub_i32 s2, s3, s2
	s_add_i32 s2, s25, s2
	s_mul_i32 s8, s2, 0x2400
	s_add_u32 s2, s21, s8
	s_addc_u32 s3, s22, 0
	s_add_u32 s8, s23, s8
	s_addc_u32 s9, s24, 0
	v_lshl_add_u64 v[128:129], s[8:9], 0, v[192:193]
	v_lshl_add_u64 v[132:133], s[8:9], 0, v[152:153]
	v_lshl_add_u64 v[136:137], s[2:3], 0, v[192:193]
	v_lshl_add_u64 v[140:141], s[2:3], 0, v[152:153]
	global_load_dwordx4 v[128:131], v[128:129], off
	s_nop 0
	global_load_dwordx4 v[132:135], v[132:133], off
	s_nop 0
	global_load_dwordx4 v[136:139], v[136:137], off
	s_nop 0
	global_load_dwordx4 v[140:143], v[140:141], off
	s_waitcnt lgkmcnt(3)
	v_mfma_f32_32x32x16_bf16 v[80:95], v[64:67], v[124:127], 0
	s_waitcnt lgkmcnt(2)
	v_mfma_f32_32x32x16_bf16 v[80:95], v[230:233], v[120:123], v[80:95]
	ds_read_b128 v[230:233], v167 offset:32768
	s_waitcnt lgkmcnt(2)
	v_mfma_f32_32x32x16_bf16 v[64:79], v[234:237], v[124:127], 0
	ds_read_b128 v[234:237], v167 offset:40960
	s_waitcnt lgkmcnt(2)
	v_mfma_f32_32x32x16_bf16 v[64:79], v[238:241], v[120:123], v[64:79]
	ds_read_b128 v[238:241], v165 offset:32768
	s_waitcnt lgkmcnt(2)
	v_mfma_f32_32x32x16_bf16 v[80:95], v[230:233], v[116:119], v[80:95]
	ds_read_b128 v[230:233], v165 offset:40960
	s_waitcnt lgkmcnt(2)
	v_mfma_f32_32x32x16_bf16 v[64:79], v[234:237], v[116:119], v[64:79]
	ds_read_b128 v[234:237], v164 offset:32768
	s_waitcnt lgkmcnt(2)
	v_mfma_f32_32x32x16_bf16 v[80:95], v[238:241], v[112:115], v[80:95]
	ds_read_b128 v[238:241], v164 offset:40960
	s_waitcnt lgkmcnt(2)
	v_mfma_f32_32x32x16_bf16 v[64:79], v[230:233], v[112:115], v[64:79]
	ds_read_b128 v[230:233], v163 offset:32768
	s_waitcnt lgkmcnt(2)
	v_mfma_f32_32x32x16_bf16 v[80:95], v[234:237], v[108:111], v[80:95]
	ds_read_b128 v[234:237], v163 offset:40960
	s_waitcnt lgkmcnt(2)
	v_mfma_f32_32x32x16_bf16 v[64:79], v[238:241], v[108:111], v[64:79]
	ds_read_b128 v[238:241], v162 offset:32768
	s_waitcnt lgkmcnt(2)
	v_mfma_f32_32x32x16_bf16 v[80:95], v[230:233], v[104:107], v[80:95]
	ds_read_b128 v[230:233], v162 offset:40960
	s_waitcnt lgkmcnt(2)
	v_mfma_f32_32x32x16_bf16 v[64:79], v[234:237], v[104:107], v[64:79]
	ds_read_b128 v[234:237], v161 offset:32768
	s_waitcnt lgkmcnt(2)
	v_mfma_f32_32x32x16_bf16 v[80:95], v[238:241], v[100:103], v[80:95]
	ds_read_b128 v[238:241], v161 offset:40960
	s_waitcnt lgkmcnt(2)
	v_mfma_f32_32x32x16_bf16 v[64:79], v[230:233], v[100:103], v[64:79]
	s_waitcnt lgkmcnt(1)
	v_mfma_f32_32x32x16_bf16 v[80:95], v[234:237], v[96:99], v[80:95]
	s_waitcnt lgkmcnt(0)
	v_mfma_f32_32x32x16_bf16 v[64:79], v[238:241], v[96:99], v[64:79]
	s_cbranch_vccnz .LBB0_652
	s_add_i32 s2, s5, s25
	s_addk_i32 s2, 0xff40
	v_cmp_lt_i32_e32 vcc, s2, v175
	v_cmp_gt_i32_e64 s[2:3], s2, v176
	s_or_b64 s[8:9], vcc, s[2:3]
	s_and_saveexec_b64 s[2:3], s[8:9]
	s_cbranch_execz .LBB0_651
	v_add_u32_e32 v242, s25, v178
	v_subrev_u32_e32 v243, 64, v242
	s_movk_i32 s8, 0x101
	v_cmp_gt_u32_e32 vcc, s8, v243
	v_subrev_u32_e32 v243, 32, v242
	s_nop 0
	v_cndmask_b32_e32 v80, v217, v80, vcc
	v_cmp_gt_u32_e32 vcc, s8, v243
	v_subrev_u32_e32 v243, 63, v242
	s_nop 0
	v_cndmask_b32_e32 v64, v217, v64, vcc
	v_cmp_gt_u32_e32 vcc, s8, v243
	v_subrev_u32_e32 v243, 31, v242
	s_nop 0
	v_cndmask_b32_e32 v81, v217, v81, vcc
	v_cmp_gt_u32_e32 vcc, s8, v243
	v_subrev_u32_e32 v243, 62, v242
	s_nop 0
	v_cndmask_b32_e32 v65, v217, v65, vcc
	v_cmp_gt_u32_e32 vcc, s8, v243
	v_subrev_u32_e32 v243, 30, v242
	s_nop 0
	v_cndmask_b32_e32 v82, v217, v82, vcc
	v_cmp_gt_u32_e32 vcc, s8, v243
	v_subrev_u32_e32 v243, 61, v242
	s_nop 0
	v_cndmask_b32_e32 v66, v217, v66, vcc
	v_cmp_gt_u32_e32 vcc, s8, v243
	v_subrev_u32_e32 v243, 29, v242
	s_nop 0
	v_cndmask_b32_e32 v83, v217, v83, vcc
	v_cmp_gt_u32_e32 vcc, s8, v243
	v_subrev_u32_e32 v243, 56, v242
	s_nop 0
	v_cndmask_b32_e32 v67, v217, v67, vcc
	v_cmp_gt_u32_e32 vcc, s8, v243
	v_subrev_u32_e32 v243, 24, v242
	s_nop 0
	v_cndmask_b32_e32 v84, v217, v84, vcc
	v_cmp_gt_u32_e32 vcc, s8, v243
	v_subrev_u32_e32 v243, 55, v242
	s_nop 0
	v_cndmask_b32_e32 v68, v217, v68, vcc
	v_cmp_gt_u32_e32 vcc, s8, v243
	v_subrev_u32_e32 v243, 23, v242
	s_nop 0
	v_cndmask_b32_e32 v85, v217, v85, vcc
	v_cmp_gt_u32_e32 vcc, s8, v243
	v_subrev_u32_e32 v243, 54, v242
	s_nop 0
	v_cndmask_b32_e32 v69, v217, v69, vcc
	v_cmp_gt_u32_e32 vcc, s8, v243
	v_subrev_u32_e32 v243, 22, v242
	s_nop 0
	v_cndmask_b32_e32 v86, v217, v86, vcc
	v_cmp_gt_u32_e32 vcc, s8, v243
	v_subrev_u32_e32 v243, 53, v242
	s_nop 0
	v_cndmask_b32_e32 v70, v217, v70, vcc
	v_cmp_gt_u32_e32 vcc, s8, v243
	v_subrev_u32_e32 v243, 21, v242
	s_nop 0
	v_cndmask_b32_e32 v87, v217, v87, vcc
	v_cmp_gt_u32_e32 vcc, s8, v243
	v_subrev_u32_e32 v243, 48, v242
	s_nop 0
	v_cndmask_b32_e32 v71, v217, v71, vcc
	v_cmp_gt_u32_e32 vcc, s8, v243
	v_add_u32_e32 v243, -16, v242
	s_nop 0
	v_cndmask_b32_e32 v88, v217, v88, vcc
	v_cmp_gt_u32_e32 vcc, s8, v243
	v_subrev_u32_e32 v243, 47, v242
	s_nop 0
	v_cndmask_b32_e32 v72, v217, v72, vcc
	v_cmp_gt_u32_e32 vcc, s8, v243
	v_add_u32_e32 v243, -15, v242
	s_nop 0
	v_cndmask_b32_e32 v89, v217, v89, vcc
	v_cmp_gt_u32_e32 vcc, s8, v243
	v_subrev_u32_e32 v243, 46, v242
	s_nop 0
	v_cndmask_b32_e32 v73, v217, v73, vcc
	v_cmp_gt_u32_e32 vcc, s8, v243
	v_add_u32_e32 v243, -14, v242
	s_nop 0
	v_cndmask_b32_e32 v90, v217, v90, vcc
	v_cmp_gt_u32_e32 vcc, s8, v243
	v_subrev_u32_e32 v243, 45, v242
	s_nop 0
	v_cndmask_b32_e32 v74, v217, v74, vcc
	v_cmp_gt_u32_e32 vcc, s8, v243
	v_add_u32_e32 v243, -13, v242
	s_nop 0
	v_cndmask_b32_e32 v91, v217, v91, vcc
	v_cmp_gt_u32_e32 vcc, s8, v243
	v_subrev_u32_e32 v243, 40, v242
	s_nop 0
	v_cndmask_b32_e32 v75, v217, v75, vcc
	v_cmp_gt_u32_e32 vcc, s8, v243
	v_add_u32_e32 v243, -8, v242
	s_nop 0
	v_cndmask_b32_e32 v92, v217, v92, vcc
	v_cmp_gt_u32_e32 vcc, s8, v243
	v_subrev_u32_e32 v243, 39, v242
	s_nop 0
	v_cndmask_b32_e32 v76, v217, v76, vcc
	v_cmp_gt_u32_e32 vcc, s8, v243
	v_add_u32_e32 v243, -7, v242
	s_nop 0
	v_cndmask_b32_e32 v93, v217, v93, vcc
	v_cmp_gt_u32_e32 vcc, s8, v243
	v_subrev_u32_e32 v243, 38, v242
	s_nop 0
	v_cndmask_b32_e32 v77, v217, v77, vcc
	v_cmp_gt_u32_e32 vcc, s8, v243
	v_add_u32_e32 v243, -6, v242
	s_nop 0
	v_cndmask_b32_e32 v94, v217, v94, vcc
	v_cmp_gt_u32_e32 vcc, s8, v243
	v_subrev_u32_e32 v243, 37, v242
	v_add_u32_e32 v242, -5, v242
	v_cndmask_b32_e32 v78, v217, v78, vcc
	v_cmp_gt_u32_e32 vcc, s8, v243
	s_nop 1
	v_cndmask_b32_e32 v95, v217, v95, vcc
	v_cmp_gt_u32_e32 vcc, s8, v242
	s_nop 1
	v_cndmask_b32_e32 v79, v217, v79, vcc

.LBB0_652:
	s_cmp_eq_u32 s100, 1
	s_cbranch_scc1 .Lwin_pvdA
	ds_read_b64_tr_b16 v[210:211], v177 offset:0
	ds_read_b64_tr_b16 v[212:213], v177 offset:0x800
	ds_read_b64_tr_b16 v[218:219], v177 offset:0x1000
	ds_read_b64_tr_b16 v[220:221], v177 offset:0x1800
	ds_read_b64_tr_b16 v[222:223], v177 offset:0x2000
	ds_read_b64_tr_b16 v[224:225], v177 offset:0x2800
	ds_read_b64_tr_b16 v[226:227], v177 offset:0x3000
	ds_read_b64_tr_b16 v[228:229], v177 offset:0x3800
	s_waitcnt lgkmcnt(0)
	s_nop 0
	v_mfma_f32_32x32x16_bf16 v[48:63], v[144:147], v[210:213], v[48:63]
	ds_read_b64_tr_b16 v[210:211], v177 offset:0x200
	ds_read_b64_tr_b16 v[212:213], v177 offset:0xa00
	v_mfma_f32_32x32x16_bf16 v[48:63], v[182:185], v[218:221], v[48:63]
	ds_read_b64_tr_b16 v[218:219], v177 offset:0x1200
	ds_read_b64_tr_b16 v[220:221], v177 offset:0x1a00
	v_mfma_f32_32x32x16_bf16 v[48:63], v[186:189], v[222:225], v[48:63]
	ds_read_b64_tr_b16 v[222:223], v177 offset:0x2200
	ds_read_b64_tr_b16 v[224:225], v177 offset:0x2a00
	v_mfma_f32_32x32x16_bf16 v[48:63], v[206:209], v[226:229], v[48:63]
	ds_read_b64_tr_b16 v[226:227], v177 offset:0x3200
	ds_read_b64_tr_b16 v[228:229], v177 offset:0x3a00
	s_waitcnt lgkmcnt(0)
	v_mfma_f32_32x32x16_bf16 v[32:47], v[144:147], v[210:213], v[32:47]
	ds_read_b64_tr_b16 v[210:211], v177 offset:0x400
	ds_read_b64_tr_b16 v[212:213], v177 offset:0xc00
	v_mfma_f32_32x32x16_bf16 v[32:47], v[182:185], v[218:221], v[32:47]
	ds_read_b64_tr_b16 v[218:219], v177 offset:0x1400
	ds_read_b64_tr_b16 v[220:221], v177 offset:0x1c00
	v_mfma_f32_32x32x16_bf16 v[32:47], v[186:189], v[222:225], v[32:47]
	ds_read_b64_tr_b16 v[222:223], v177 offset:0x2400
	ds_read_b64_tr_b16 v[224:225], v177 offset:0x2c00
	v_mfma_f32_32x32x16_bf16 v[32:47], v[206:209], v[226:229], v[32:47]
	ds_read_b64_tr_b16 v[226:227], v177 offset:0x3400
	ds_read_b64_tr_b16 v[228:229], v177 offset:0x3c00
	s_waitcnt lgkmcnt(0)
	v_mfma_f32_32x32x16_bf16 v[16:31], v[144:147], v[210:213], v[16:31]
	ds_read_b64_tr_b16 v[210:211], v177 offset:0x600
	ds_read_b64_tr_b16 v[212:213], v177 offset:0xe00
	v_mfma_f32_32x32x16_bf16 v[16:31], v[182:185], v[218:221], v[16:31]
	ds_read_b64_tr_b16 v[218:219], v177 offset:0x1600
	ds_read_b64_tr_b16 v[220:221], v177 offset:0x1e00
	v_mfma_f32_32x32x16_bf16 v[16:31], v[186:189], v[222:225], v[16:31]
	ds_read_b64_tr_b16 v[222:223], v177 offset:0x2600
	ds_read_b64_tr_b16 v[224:225], v177 offset:0x2e00
	v_mfma_f32_32x32x16_bf16 v[16:31], v[206:209], v[226:229], v[16:31]
	ds_read_b64_tr_b16 v[226:227], v177 offset:0x3600
	ds_read_b64_tr_b16 v[228:229], v177 offset:0x3e00
	s_waitcnt lgkmcnt(0)
	v_mfma_f32_32x32x16_bf16 v[0:15], v[144:147], v[210:213], v[0:15]
	v_max_f32_e32 v144, v81, v81
	v_max_f32_e32 v145, v80, v80
	v_max_f32_e32 v144, v145, v144
	v_max3_f32 v144, v144, v82, v83
	v_max3_f32 v144, v144, v84, v85
	v_max3_f32 v144, v144, v86, v87
	v_max3_f32 v144, v144, v88, v89
	v_max3_f32 v144, v144, v90, v91
	v_max3_f32 v144, v144, v92, v93
	v_mfma_f32_32x32x16_bf16 v[0:15], v[182:185], v[218:221], v[0:15]
	v_max3_f32 v144, v144, v94, v95
	v_max3_f32 v144, v144, v64, v65
	v_max3_f32 v144, v144, v66, v67
	v_max3_f32 v144, v144, v68, v69
	v_max3_f32 v144, v144, v70, v71
	v_max3_f32 v144, v144, v72, v73
	v_max3_f32 v144, v144, v74, v75
	v_max3_f32 v144, v144, v76, v77
	v_mfma_f32_32x32x16_bf16 v[0:15], v[186:189], v[222:225], v[0:15]
	v_max3_f32 v144, v144, v78, v79
	v_mov_b32_e32 v145, v144
	s_nop 1
	v_permlane32_swap_b32_e32 v144, v145
	v_max_f32_e32 v145, v145, v145
	v_max_f32_e32 v144, v144, v144
	v_max_f32_e32 v144, v144, v145
	v_sub_f32_e32 v145, v144, v174
	s_mov_b32 s2, 0x42b504f3
	v_cmp_ge_f32_e32 vcc, s2, v145
	v_max_f32_e32 v145, v174, v174
	v_max_f32_e32 v145, v145, v144
	v_mfma_f32_32x32x16_bf16 v[0:15], v[206:209], v[226:229], v[0:15]
	v_sub_f32_e32 v144, v174, v145
	v_mul_f32_e32 v144, 0x3e0293ee, v144
	v_exp_f32_e32 v144, v144
	s_cmp_eq_u64 vcc, exec
	s_cselect_b64 s[2:3], -1, 0
.Lwin_pvjA:
	s_barrier
	s_waitcnt vmcnt(0)
	v_cndmask_b32_e64 v144, v144, 1.0, s[2:3]
	v_cmp_gt_f32_e32 vcc, 1.0, v144
	s_waitcnt vmcnt(3)
	ds_write_b128 v169, v[128:131] offset:16384
	s_waitcnt vmcnt(2)
	ds_write_b128 v170, v[132:135] offset:16384
	s_waitcnt vmcnt(1)
	ds_write_b128 v171, v[136:139] offset:49152
	s_waitcnt vmcnt(0)
	ds_write_b128 v172, v[140:143] offset:49152
	s_cbranch_vccz .LBB0_656
	s_and_saveexec_b64 s[8:9], s[0:1]
	ds_write_b32 v158, v144 offset:128
	s_or_b64 exec, exec, s[8:9]
	s_waitcnt lgkmcnt(0)
	v_add_u32_e32 v140, v151, v150
	ds_read_b128 v[128:131], v140 offset:224
	ds_read_b128 v[132:135], v140 offset:192
	ds_read_b128 v[136:139], v140 offset:128
	ds_read_b128 v[140:143], v140 offset:160
	s_waitcnt lgkmcnt(3)
	v_pk_mul_f32 v[62:63], v[62:63], v[130:131]
	v_pk_mul_f32 v[60:61], v[60:61], v[128:129]
	s_waitcnt lgkmcnt(2)
	v_pk_mul_f32 v[58:59], v[58:59], v[134:135]
	v_pk_mul_f32 v[56:57], v[56:57], v[132:133]
	s_waitcnt lgkmcnt(0)
	v_pk_mul_f32 v[54:55], v[54:55], v[142:143]
	v_pk_mul_f32 v[52:53], v[52:53], v[140:141]
	v_pk_mul_f32 v[50:51], v[50:51], v[138:139]
	v_pk_mul_f32 v[48:49], v[48:49], v[136:137]
	v_pk_mul_f32 v[46:47], v[46:47], v[130:131]
	v_pk_mul_f32 v[44:45], v[44:45], v[128:129]
	v_pk_mul_f32 v[42:43], v[42:43], v[134:135]
	v_pk_mul_f32 v[40:41], v[40:41], v[132:133]
	v_pk_mul_f32 v[38:39], v[38:39], v[142:143]
	v_pk_mul_f32 v[36:37], v[36:37], v[140:141]
	v_pk_mul_f32 v[34:35], v[34:35], v[138:139]
	v_pk_mul_f32 v[32:33], v[32:33], v[136:137]
	v_pk_mul_f32 v[30:31], v[30:31], v[130:131]
	v_pk_mul_f32 v[28:29], v[28:29], v[128:129]
	v_pk_mul_f32 v[26:27], v[26:27], v[134:135]
	v_pk_mul_f32 v[24:25], v[24:25], v[132:133]
	v_pk_mul_f32 v[22:23], v[22:23], v[142:143]
	v_pk_mul_f32 v[20:21], v[20:21], v[140:141]
	v_pk_mul_f32 v[18:19], v[18:19], v[138:139]
	v_pk_mul_f32 v[16:17], v[16:17], v[136:137]
	v_pk_mul_f32 v[14:15], v[14:15], v[130:131]
	v_pk_mul_f32 v[12:13], v[12:13], v[128:129]
	v_pk_mul_f32 v[10:11], v[10:11], v[134:135]
	v_pk_mul_f32 v[8:9], v[8:9], v[132:133]
	v_pk_mul_f32 v[6:7], v[6:7], v[142:143]
	v_pk_mul_f32 v[4:5], v[4:5], v[140:141]
	v_pk_mul_f32 v[2:3], v[2:3], v[138:139]
	v_pk_mul_f32 v[0:1], v[0:1], v[136:137]

.Lwin_deadA:
	v_add_f32_e32 v144, 0, v191
	v_add_f32_e32 v144, v201, v144
	v_add_f32_e32 v144, v145, v144
	v_add_f32_e32 v144, v200, v144
	v_add_f32_e32 v144, v146, v144
	v_add_f32_e32 v144, v190, v144
	v_add_f32_e32 v144, v147, v144
	v_add_f32_e32 v144, v189, v144
	v_add_f32_e32 v144, v186, v144
	v_add_f32_e32 v144, v188, v144
	v_add_f32_e32 v144, v185, v144
	v_add_f32_e32 v144, v187, v144
	v_exp_f32_e32 v142, v142
	v_add_f32_e32 v144, v182, v144
	v_exp_f32_e32 v143, v143
	v_add_f32_e32 v144, v184, v144
	v_exp_f32_e32 v140, v140
	v_add_f32_e32 v144, v181, v144
	v_exp_f32_e32 v141, v141
	v_add_f32_e32 v144, v183, v144
	v_exp_f32_e32 v138, v138
	v_add_f32_e32 v144, v142, v144
	v_exp_f32_e32 v139, v139
	v_add_f32_e32 v144, v143, v144
	v_exp_f32_e32 v136, v136
	v_add_f32_e32 v144, v140, v144
	v_exp_f32_e32 v137, v137
	v_add_f32_e32 v144, v141, v144
	v_exp_f32_e32 v134, v134
	v_add_f32_e32 v144, v138, v144
	v_exp_f32_e32 v135, v135
	v_add_f32_e32 v144, v139, v144
	v_exp_f32_e32 v132, v132
	v_add_f32_e32 v144, v136, v144
	v_exp_f32_e32 v133, v133
	v_add_f32_e32 v144, v137, v144
	v_exp_f32_e32 v130, v130
	v_add_f32_e32 v144, v134, v144
	v_exp_f32_e32 v131, v131
	v_add_f32_e32 v144, v135, v144
	v_exp_f32_e32 v128, v128
	v_add_f32_e32 v144, v132, v144
	v_exp_f32_e32 v129, v129
	v_add_f32_e32 v144, v133, v144
	v_add_f32_e32 v144, v130, v144
	v_add_f32_e32 v144, v131, v144
	v_add_f32_e32 v144, v128, v144
	v_add_f32_e32 v179, v129, v144
	v_mov_b32_e32 v180, v179
	v_cvt_pk_bf16_f32 v144, v191, v201
	v_cvt_pk_bf16_f32 v145, v145, v200
	v_cvt_pk_bf16_f32 v146, v146, v190
	v_cvt_pk_bf16_f32 v147, v147, v189
	v_cvt_pk_bf16_f32 v186, v186, v188
	v_cvt_pk_bf16_f32 v187, v185, v187
	v_cvt_pk_bf16_f32 v188, v182, v184
	v_cvt_pk_bf16_f32 v189, v181, v183
	v_cvt_pk_bf16_f32 v182, v142, v143
	v_cvt_pk_bf16_f32 v183, v140, v141
	v_cvt_pk_bf16_f32 v184, v138, v139
	v_cvt_pk_bf16_f32 v185, v136, v137
	v_cvt_pk_bf16_f32 v200, v134, v135
	v_cvt_pk_bf16_f32 v201, v132, v133
	v_cvt_pk_bf16_f32 v202, v130, v131
	s_nop 0
	v_permlane32_swap_b32_e32 v179, v180
	v_permlane32_swap_b32_e32 v144, v146
	v_cvt_pk_bf16_f32 v203, v128, v129
	v_permlane32_swap_b32_e32 v200, v202
	v_permlane32_swap_b32_e32 v145, v147
	v_permlane32_swap_b32_e32 v186, v188
	v_permlane32_swap_b32_e32 v187, v189
	v_permlane32_swap_b32_e32 v182, v184
	v_permlane32_swap_b32_e32 v183, v185
	v_permlane32_swap_b32_e32 v201, v203
	s_add_i32 s2, s27, 3
	s_cmp_lt_i32 s2, s20
	s_cselect_b64 s[8:9], -1, 0
	s_and_b64 s[2:3], s[8:9], exec
	s_cselect_b32 s2, 0, s20
	s_cselect_b32 s3, s19, 0x4000
	s_lshl_b32 s2, s2, 6
	s_sub_i32 s2, s3, s2
	s_add_i32 s2, s25, s2
	s_mulk_i32 s2, 0x2400
	s_add_i32 s10, s2, 0xfff70000
	s_add_u32 s2, s21, s10
	s_addc_u32 s3, s22, 0
	s_add_u32 s10, s23, s10
	s_addc_u32 s11, s24, 0
	v_lshl_add_u64 v[128:129], s[10:11], 0, v[192:193]
	v_lshl_add_u64 v[132:133], s[10:11], 0, v[152:153]
	v_lshl_add_u64 v[136:137], s[2:3], 0, v[192:193]
	v_lshl_add_u64 v[140:141], s[2:3], 0, v[152:153]
	global_load_dwordx4 v[128:131], v[128:129], off
	s_nop 0
	global_load_dwordx4 v[132:135], v[132:133], off
	s_nop 0
	global_load_dwordx4 v[136:139], v[136:137], off
	s_nop 0
	global_load_dwordx4 v[140:143], v[140:141], off
	v_mov_b32_e32 v64, v217
	v_mov_b32_e32 v65, v217
	v_mov_b32_e32 v66, v217
	v_mov_b32_e32 v67, v217
	v_mov_b32_e32 v68, v217
	v_mov_b32_e32 v69, v217
	v_mov_b32_e32 v70, v217
	v_mov_b32_e32 v71, v217
	v_mov_b32_e32 v72, v217
	v_mov_b32_e32 v73, v217
	v_mov_b32_e32 v74, v217
	v_mov_b32_e32 v75, v217
	v_mov_b32_e32 v76, v217
	v_mov_b32_e32 v77, v217
	v_mov_b32_e32 v78, v217
	v_mov_b32_e32 v79, v217
	v_mov_b32_e32 v80, v217
	v_mov_b32_e32 v81, v217
	v_mov_b32_e32 v82, v217
	v_mov_b32_e32 v83, v217
	v_mov_b32_e32 v84, v217
	v_mov_b32_e32 v85, v217
	v_mov_b32_e32 v86, v217
	v_mov_b32_e32 v87, v217
	v_mov_b32_e32 v88, v217
	v_mov_b32_e32 v89, v217
	v_mov_b32_e32 v90, v217
	v_mov_b32_e32 v91, v217
	v_mov_b32_e32 v92, v217
	v_mov_b32_e32 v93, v217
	v_mov_b32_e32 v94, v217
	v_mov_b32_e32 v95, v217
	s_mov_b32 s100, 1
	s_branch .LBB0_644
.Lwin_deadB:
	s_andn2_b64 vcc, exec, s[8:9]
	v_exp_f32_e32 v215, v144
	v_add_f32_e32 v144, 0, v141
	v_add_f32_e32 v144, v143, v144
	v_add_f32_e32 v144, v139, v144
	v_add_f32_e32 v144, v142, v144
	v_add_f32_e32 v144, v137, v144
	v_add_f32_e32 v144, v140, v144
	v_add_f32_e32 v144, v136, v144
	v_add_f32_e32 v144, v138, v144
	v_add_f32_e32 v144, v133, v144
	v_add_f32_e32 v144, v135, v144
	v_add_f32_e32 v144, v131, v144
	v_add_f32_e32 v144, v134, v144
	v_exp_f32_e32 v201, v145
	v_add_f32_e32 v144, v129, v144
	v_exp_f32_e32 v205, v146
	v_add_f32_e32 v144, v132, v144
	v_exp_f32_e32 v206, v147
	v_add_f32_e32 v144, v128, v144
	v_exp_f32_e32 v181, v181
	v_add_f32_e32 v144, v130, v144
	v_exp_f32_e32 v207, v182
	v_add_f32_e32 v144, v201, v144
	v_exp_f32_e32 v208, v183
	v_add_f32_e32 v144, v205, v144
	v_exp_f32_e32 v209, v184
	v_add_f32_e32 v144, v206, v144
	v_exp_f32_e32 v210, v185
	v_add_f32_e32 v144, v181, v144
	v_exp_f32_e32 v211, v186
	v_add_f32_e32 v144, v207, v144
	v_exp_f32_e32 v212, v187
	v_add_f32_e32 v144, v208, v144
	v_exp_f32_e32 v213, v188
	v_add_f32_e32 v144, v209, v144
	v_exp_f32_e32 v214, v189
	v_add_f32_e32 v144, v210, v144
	v_exp_f32_e32 v190, v190
	v_add_f32_e32 v144, v211, v144
	v_exp_f32_e32 v191, v191
	v_add_f32_e32 v144, v212, v144
	v_exp_f32_e32 v200, v200
	v_add_f32_e32 v144, v213, v144
	v_add_f32_e32 v144, v214, v144
	v_add_f32_e32 v144, v190, v144
	v_add_f32_e32 v144, v191, v144
	v_add_f32_e32 v144, v200, v144
	v_add_f32_e32 v203, v215, v144
	v_mov_b32_e32 v204, v203
	v_cvt_pk_bf16_f32 v144, v141, v143
	v_cvt_pk_bf16_f32 v145, v139, v142
	v_cvt_pk_bf16_f32 v146, v137, v140
	v_cvt_pk_bf16_f32 v147, v136, v138
	s_nop 1
	v_permlane32_swap_b32_e32 v203, v204
	v_permlane32_swap_b32_e32 v144, v146
	v_permlane32_swap_b32_e32 v145, v147
	v_cvt_pk_bf16_f32 v182, v133, v135
	v_cvt_pk_bf16_f32 v183, v131, v134
	v_cvt_pk_bf16_f32 v184, v129, v132
	v_cvt_pk_bf16_f32 v185, v128, v130
	v_cvt_pk_bf16_f32 v186, v201, v205
	v_cvt_pk_bf16_f32 v187, v206, v181
	v_cvt_pk_bf16_f32 v188, v207, v208
	v_cvt_pk_bf16_f32 v189, v209, v210
	v_cvt_pk_bf16_f32 v206, v211, v212
	v_cvt_pk_bf16_f32 v207, v213, v214
	v_cvt_pk_bf16_f32 v208, v190, v191
	v_cvt_pk_bf16_f32 v209, v200, v215
	s_nop 0
	v_permlane32_swap_b32_e32 v182, v184
	v_permlane32_swap_b32_e32 v183, v185
	v_permlane32_swap_b32_e32 v186, v188
	v_permlane32_swap_b32_e32 v187, v189
	v_permlane32_swap_b32_e32 v206, v208
	v_permlane32_swap_b32_e32 v207, v209
	s_add_i32 s2, s27, 4
	s_cmp_lt_i32 s2, s20
	s_cselect_b32 s2, 0, s20
	s_cselect_b32 s3, s19, 0x4000
	s_lshl_b32 s2, s2, 6
	s_sub_i32 s2, s3, s2
	s_add_i32 s2, s25, s2
	s_mul_i32 s8, s2, 0x2400
	s_add_u32 s2, s21, s8
	s_addc_u32 s3, s22, 0
	s_add_u32 s8, s23, s8
	s_addc_u32 s9, s24, 0
	v_lshl_add_u64 v[128:129], s[8:9], 0, v[192:193]
	v_lshl_add_u64 v[132:133], s[8:9], 0, v[152:153]
	v_lshl_add_u64 v[136:137], s[2:3], 0, v[192:193]
	v_lshl_add_u64 v[140:141], s[2:3], 0, v[152:153]
	global_load_dwordx4 v[128:131], v[128:129], off
	s_nop 0
	global_load_dwordx4 v[132:135], v[132:133], off
	s_nop 0
	global_load_dwordx4 v[136:139], v[136:137], off
	s_nop 0
	global_load_dwordx4 v[140:143], v[140:141], off
	v_mov_b32_e32 v64, v217
	v_mov_b32_e32 v65, v217
	v_mov_b32_e32 v66, v217
	v_mov_b32_e32 v67, v217
	v_mov_b32_e32 v68, v217
	v_mov_b32_e32 v69, v217
	v_mov_b32_e32 v70, v217
	v_mov_b32_e32 v71, v217
	v_mov_b32_e32 v72, v217
	v_mov_b32_e32 v73, v217
	v_mov_b32_e32 v74, v217
	v_mov_b32_e32 v75, v217
	v_mov_b32_e32 v76, v217
	v_mov_b32_e32 v77, v217
	v_mov_b32_e32 v78, v217
	v_mov_b32_e32 v79, v217
	v_mov_b32_e32 v80, v217
	v_mov_b32_e32 v81, v217
	v_mov_b32_e32 v82, v217
	v_mov_b32_e32 v83, v217
	v_mov_b32_e32 v84, v217
	v_mov_b32_e32 v85, v217
	v_mov_b32_e32 v86, v217
	v_mov_b32_e32 v87, v217
	v_mov_b32_e32 v88, v217
	v_mov_b32_e32 v89, v217
	v_mov_b32_e32 v90, v217
	v_mov_b32_e32 v91, v217
	v_mov_b32_e32 v92, v217
	v_mov_b32_e32 v93, v217
	v_mov_b32_e32 v94, v217
	v_mov_b32_e32 v95, v217
	s_mov_b32 s101, 1
	s_branch .LBB0_652
.Lwin_pvdA:
	v_max_f32_e32 v144, v81, v81
	v_max_f32_e32 v145, v80, v80
	v_max_f32_e32 v144, v145, v144
	v_max3_f32 v144, v144, v82, v83
	v_max3_f32 v144, v144, v84, v85
	v_max3_f32 v144, v144, v86, v87
	v_max3_f32 v144, v144, v88, v89
	v_max3_f32 v144, v144, v90, v91
	v_max3_f32 v144, v144, v92, v93
	v_max3_f32 v144, v144, v94, v95
	v_max3_f32 v144, v144, v64, v65
	v_max3_f32 v144, v144, v66, v67
	v_max3_f32 v144, v144, v68, v69
	v_max3_f32 v144, v144, v70, v71
	v_max3_f32 v144, v144, v72, v73
	v_max3_f32 v144, v144, v74, v75
	v_max3_f32 v144, v144, v76, v77
	v_max3_f32 v144, v144, v78, v79
	v_mov_b32_e32 v145, v144
	s_nop 1
	v_permlane32_swap_b32_e32 v144, v145
	v_max_f32_e32 v145, v145, v145
	v_max_f32_e32 v144, v144, v144
	v_max_f32_e32 v144, v144, v145
	v_sub_f32_e32 v145, v144, v174
	s_mov_b32 s2, 0x42b504f3
	v_cmp_ge_f32_e32 vcc, s2, v145
	v_max_f32_e32 v145, v174, v174
	v_max_f32_e32 v145, v145, v144
	v_sub_f32_e32 v144, v174, v145
	v_mul_f32_e32 v144, 0x3e0293ee, v144
	v_exp_f32_e32 v144, v144
	s_cmp_eq_u64 vcc, exec
	s_cselect_b64 s[2:3], -1, 0
	s_branch .Lwin_pvjA
.Lwin_pvdB:
	v_max_f32_e32 v144, v81, v81
	v_max_f32_e32 v145, v80, v80
	v_max_f32_e32 v144, v145, v144
	v_max3_f32 v144, v144, v82, v83
	v_max3_f32 v144, v144, v84, v85
	v_max3_f32 v144, v144, v86, v87
	v_max3_f32 v144, v144, v88, v89
	v_max3_f32 v144, v144, v90, v91
	v_max3_f32 v144, v144, v92, v93
	v_max3_f32 v144, v144, v94, v95
	v_max3_f32 v144, v144, v64, v65
	v_max3_f32 v144, v144, v66, v67
	v_max3_f32 v144, v144, v68, v69
	v_max3_f32 v144, v144, v70, v71
	v_max3_f32 v144, v144, v72, v73
	v_max3_f32 v144, v144, v74, v75
	v_max3_f32 v144, v144, v76, v77
	v_max3_f32 v144, v144, v78, v79
	v_mov_b32_e32 v145, v144
	s_nop 1
	v_permlane32_swap_b32_e32 v144, v145
	v_max_f32_e32 v145, v145, v145
	v_max_f32_e32 v144, v144, v144
	v_max_f32_e32 v144, v144, v145
	v_sub_f32_e32 v145, v144, v174
	s_mov_b32 s2, 0x42b504f3
	v_cmp_ge_f32_e32 vcc, s2, v145
	v_max_f32_e32 v145, v174, v174
	v_max_f32_e32 v144, v145, v144
	v_sub_f32_e32 v145, v174, v144
	v_mul_f32_e32 v145, 0x3e0293ee, v145
	v_exp_f32_e32 v145, v145
	s_cmp_eq_u64 vcc, exec
	s_cselect_b64 s[2:3], -1, 0
	s_branch .Lwin_pvjB

.LBB0_659:
	s_mov_b32 s101, 0
	s_ashr_i32 s5, s4, 31
	v_readlane_b32 s22, v254, 48
	ds_read_b128 v[64:67], v166 offset:49152
	ds_read_b128 v[68:71], v166 offset:57344
	s_waitcnt lgkmcnt(1)
	v_mfma_f32_32x32x16_bf16 v[80:95], v[64:67], v[124:127], 0
	s_waitcnt lgkmcnt(0)
	v_mfma_f32_32x32x16_bf16 v[64:79], v[68:71], v[124:127], 0
	ds_read_b128 v[124:127], v168 offset:49152
	ds_read_b128 v[168:171], v168 offset:57344
	s_waitcnt lgkmcnt(1)
	v_mfma_f32_32x32x16_bf16 v[80:95], v[124:127], v[120:123], v[80:95]
	s_waitcnt lgkmcnt(0)
	v_mfma_f32_32x32x16_bf16 v[64:79], v[168:171], v[120:123], v[64:79]
	ds_read_b128 v[120:123], v167 offset:49152
	ds_read_b128 v[124:127], v167 offset:57344
	s_waitcnt lgkmcnt(1)
	v_mfma_f32_32x32x16_bf16 v[80:95], v[120:123], v[116:119], v[80:95]
	s_waitcnt lgkmcnt(0)
	v_mfma_f32_32x32x16_bf16 v[64:79], v[124:127], v[116:119], v[64:79]
	ds_read_b128 v[116:119], v165 offset:49152
	ds_read_b128 v[120:123], v165 offset:57344
	s_waitcnt lgkmcnt(1)
	v_mfma_f32_32x32x16_bf16 v[80:95], v[116:119], v[112:115], v[80:95]
	s_waitcnt lgkmcnt(0)
	v_mfma_f32_32x32x16_bf16 v[64:79], v[120:123], v[112:115], v[64:79]
	ds_read_b128 v[112:115], v164 offset:49152
	ds_read_b128 v[116:119], v164 offset:57344
	v_exp_f32_e32 v120, v128
	v_exp_f32_e32 v121, v129
	s_waitcnt lgkmcnt(1)
	v_mfma_f32_32x32x16_bf16 v[80:95], v[112:115], v[108:111], v[80:95]
	s_waitcnt lgkmcnt(0)
	v_mfma_f32_32x32x16_bf16 v[64:79], v[116:119], v[108:111], v[64:79]
	ds_read_b128 v[108:111], v163 offset:49152
	ds_read_b128 v[112:115], v163 offset:57344
	v_exp_f32_e32 v116, v132
	v_exp_f32_e32 v117, v133
	v_exp_f32_e32 v118, v130
	v_exp_f32_e32 v119, v131
	s_waitcnt lgkmcnt(1)
	v_mfma_f32_32x32x16_bf16 v[80:95], v[108:111], v[104:107], v[80:95]
	s_waitcnt lgkmcnt(0)
	v_mfma_f32_32x32x16_bf16 v[64:79], v[112:115], v[104:107], v[64:79]
	ds_read_b128 v[104:107], v162 offset:49152
	ds_read_b128 v[108:111], v162 offset:57344
	v_exp_f32_e32 v112, v136
	v_exp_f32_e32 v113, v137
	v_exp_f32_e32 v114, v134
	v_exp_f32_e32 v115, v135
	s_waitcnt lgkmcnt(1)
	v_mfma_f32_32x32x16_bf16 v[80:95], v[104:107], v[100:103], v[80:95]
	s_waitcnt lgkmcnt(0)
	v_mfma_f32_32x32x16_bf16 v[64:79], v[108:111], v[100:103], v[64:79]
	ds_read_b128 v[100:103], v161 offset:49152
	ds_read_b128 v[104:107], v161 offset:57344
	v_exp_f32_e32 v108, v140
	v_exp_f32_e32 v109, v141
	v_exp_f32_e32 v110, v138
	v_exp_f32_e32 v111, v139
	s_waitcnt lgkmcnt(1)
	v_mfma_f32_32x32x16_bf16 v[80:95], v[100:103], v[96:99], v[80:95]
	s_waitcnt lgkmcnt(0)
	v_mfma_f32_32x32x16_bf16 v[64:79], v[104:107], v[96:99], v[64:79]
	v_add_f32_e32 v96, 0, v191
	v_add_f32_e32 v96, v201, v96
	v_add_f32_e32 v96, v145, v96
	v_add_f32_e32 v96, v200, v96
	v_add_f32_e32 v96, v146, v96
	v_add_f32_e32 v96, v190, v96
	v_add_f32_e32 v96, v147, v96
	v_add_f32_e32 v96, v189, v96
	v_add_f32_e32 v96, v186, v96
	v_add_f32_e32 v96, v188, v96
	v_add_f32_e32 v96, v185, v96
	v_add_f32_e32 v96, v187, v96
	v_exp_f32_e32 v106, v142
	v_add_f32_e32 v96, v182, v96
	v_exp_f32_e32 v107, v143
	v_add_f32_e32 v96, v184, v96
	v_add_f32_e32 v96, v181, v96
	v_add_f32_e32 v96, v183, v96
	v_add_f32_e32 v96, v106, v96
	v_add_f32_e32 v96, v107, v96
	v_add_f32_e32 v96, v108, v96
	v_add_f32_e32 v96, v109, v96
	v_add_f32_e32 v96, v110, v96
	v_add_f32_e32 v96, v111, v96
	v_add_f32_e32 v96, v112, v96
	v_add_f32_e32 v96, v113, v96
	v_add_f32_e32 v96, v114, v96
	v_add_f32_e32 v96, v115, v96
	v_add_f32_e32 v96, v116, v96
	v_add_f32_e32 v96, v117, v96
	v_add_f32_e32 v96, v118, v96
	v_add_f32_e32 v96, v119, v96
	v_add_f32_e32 v96, v120, v96
	v_add_f32_e32 v96, v121, v96
	v_mov_b32_e32 v97, v96
	v_cvt_pk_bf16_f32 v98, v191, v201
	v_cvt_pk_bf16_f32 v99, v145, v200
	v_cvt_pk_bf16_f32 v100, v146, v190
	v_cvt_pk_bf16_f32 v101, v147, v189
	s_nop 1
	v_permlane32_swap_b32_e32 v96, v97
	v_permlane32_swap_b32_e32 v98, v100
	v_permlane32_swap_b32_e32 v99, v101
	v_cvt_pk_bf16_f32 v102, v186, v188
	v_cvt_pk_bf16_f32 v103, v185, v187
	v_cvt_pk_bf16_f32 v104, v182, v184
	v_cvt_pk_bf16_f32 v105, v181, v183
	v_cvt_pk_bf16_f32 v106, v106, v107
	v_cvt_pk_bf16_f32 v107, v108, v109
	v_cvt_pk_bf16_f32 v108, v110, v111
	v_cvt_pk_bf16_f32 v109, v112, v113
	v_cvt_pk_bf16_f32 v110, v114, v115
	v_cvt_pk_bf16_f32 v111, v116, v117
	v_cvt_pk_bf16_f32 v112, v118, v119
	v_cvt_pk_bf16_f32 v113, v120, v121
	s_nop 0
	v_permlane32_swap_b32_e32 v102, v104
	v_permlane32_swap_b32_e32 v103, v105
	v_permlane32_swap_b32_e32 v106, v108
	v_permlane32_swap_b32_e32 v107, v109
	v_permlane32_swap_b32_e32 v110, v112
	v_permlane32_swap_b32_e32 v111, v113
	ds_read_b64_tr_b16 v[114:115], v160 offset:0
	ds_read_b64_tr_b16 v[116:117], v160 offset:0x800
	ds_read_b64_tr_b16 v[118:119], v160 offset:0x1000
	ds_read_b64_tr_b16 v[120:121], v160 offset:0x1800
	ds_read_b64_tr_b16 v[122:123], v160 offset:0x2000
	ds_read_b64_tr_b16 v[124:125], v160 offset:0x2800
	ds_read_b64_tr_b16 v[126:127], v160 offset:0x3000
	ds_read_b64_tr_b16 v[128:129], v160 offset:0x3800
	s_waitcnt lgkmcnt(0)
	s_nop 0
	v_mfma_f32_32x32x16_bf16 v[48:63], v[98:101], v[114:117], v[48:63]
	ds_read_b64_tr_b16 v[114:115], v160 offset:0x200
	ds_read_b64_tr_b16 v[116:117], v160 offset:0xa00
	v_mfma_f32_32x32x16_bf16 v[48:63], v[102:105], v[118:121], v[48:63]
	ds_read_b64_tr_b16 v[118:119], v160 offset:0x1200
	ds_read_b64_tr_b16 v[120:121], v160 offset:0x1a00
	v_mfma_f32_32x32x16_bf16 v[48:63], v[106:109], v[122:125], v[48:63]
	ds_read_b64_tr_b16 v[122:123], v160 offset:0x2200
	ds_read_b64_tr_b16 v[124:125], v160 offset:0x2a00
	v_mfma_f32_32x32x16_bf16 v[48:63], v[110:113], v[126:129], v[48:63]
	ds_read_b64_tr_b16 v[126:127], v160 offset:0x3200
	ds_read_b64_tr_b16 v[128:129], v160 offset:0x3a00
	s_waitcnt lgkmcnt(0)
	v_mfma_f32_32x32x16_bf16 v[32:47], v[98:101], v[114:117], v[32:47]
	ds_read_b64_tr_b16 v[114:115], v160 offset:0x400
	ds_read_b64_tr_b16 v[116:117], v160 offset:0xc00
	v_mfma_f32_32x32x16_bf16 v[32:47], v[102:105], v[118:121], v[32:47]
	ds_read_b64_tr_b16 v[118:119], v160 offset:0x1400
	ds_read_b64_tr_b16 v[120:121], v160 offset:0x1c00
	v_mfma_f32_32x32x16_bf16 v[32:47], v[106:109], v[122:125], v[32:47]
	ds_read_b64_tr_b16 v[122:123], v160 offset:0x2400
	ds_read_b64_tr_b16 v[124:125], v160 offset:0x2c00
	v_mfma_f32_32x32x16_bf16 v[32:47], v[110:113], v[126:129], v[32:47]
	ds_read_b64_tr_b16 v[126:127], v160 offset:0x3400
	ds_read_b64_tr_b16 v[128:129], v160 offset:0x3c00
	s_waitcnt lgkmcnt(0)
	v_mfma_f32_32x32x16_bf16 v[16:31], v[98:101], v[114:117], v[16:31]
	ds_read_b64_tr_b16 v[114:115], v160 offset:0x600
	ds_read_b64_tr_b16 v[116:117], v160 offset:0xe00
	v_mfma_f32_32x32x16_bf16 v[16:31], v[102:105], v[118:121], v[16:31]
	ds_read_b64_tr_b16 v[118:119], v160 offset:0x1600
	ds_read_b64_tr_b16 v[120:121], v160 offset:0x1e00
	v_mfma_f32_32x32x16_bf16 v[16:31], v[106:109], v[122:125], v[16:31]
	ds_read_b64_tr_b16 v[122:123], v160 offset:0x2600
	ds_read_b64_tr_b16 v[124:125], v160 offset:0x2e00
	v_mfma_f32_32x32x16_bf16 v[16:31], v[110:113], v[126:129], v[16:31]
	ds_read_b64_tr_b16 v[126:127], v160 offset:0x3600
	ds_read_b64_tr_b16 v[128:129], v160 offset:0x3e00
	s_waitcnt lgkmcnt(0)
	v_mfma_f32_32x32x16_bf16 v[0:15], v[98:101], v[114:117], v[0:15]
	v_max_f32_e32 v98, v81, v81
	v_max_f32_e32 v99, v80, v80
	v_max_f32_e32 v98, v99, v98
	v_max3_f32 v98, v98, v82, v83
	v_max3_f32 v98, v98, v84, v85
	v_max3_f32 v98, v98, v86, v87
	v_max3_f32 v98, v98, v88, v89
	v_max3_f32 v98, v98, v90, v91
	v_max3_f32 v98, v98, v92, v93
	v_mfma_f32_32x32x16_bf16 v[0:15], v[102:105], v[118:121], v[0:15]
	v_max3_f32 v98, v98, v94, v95
	v_max3_f32 v98, v98, v64, v65
	v_max3_f32 v98, v98, v66, v67
	v_max3_f32 v98, v98, v68, v69
	v_max3_f32 v98, v98, v70, v71
	v_max3_f32 v98, v98, v72, v73
	v_max3_f32 v98, v98, v74, v75
	v_max3_f32 v98, v98, v76, v77
	v_mfma_f32_32x32x16_bf16 v[0:15], v[106:109], v[122:125], v[0:15]
	v_max3_f32 v98, v98, v78, v79
	v_mov_b32_e32 v99, v98
	s_nop 1
	v_permlane32_swap_b32_e32 v98, v99
	v_max_f32_e32 v99, v99, v99
	v_max_f32_e32 v98, v98, v98
	v_max_f32_e32 v98, v98, v99
	v_sub_f32_e32 v99, v98, v174
	s_mov_b32 s0, 0x42b504f3
	v_cmp_ge_f32_e32 vcc, s0, v99
	v_max_f32_e32 v99, v174, v174
	v_max_f32_e32 v99, v99, v98
	v_mfma_f32_32x32x16_bf16 v[0:15], v[110:113], v[126:129], v[0:15]
	v_sub_f32_e32 v98, v174, v99
	v_mul_f32_e32 v98, 0x3e0293ee, v98
	v_exp_f32_e32 v98, v98
	s_cmp_eq_u64 vcc, exec
	s_cselect_b64 s[0:1], -1, 0
	v_cndmask_b32_e64 v98, v98, 1.0, s[0:1]
	v_cmp_gt_f32_e32 vcc, 1.0, v98
	s_barrier
	s_cbranch_vccz .LBB0_663
	v_cmp_gt_u32_e32 vcc, 32, v156
	s_and_saveexec_b64 s[2:3], vcc
	ds_write_b32 v158, v98 offset:128
	s_or_b64 exec, exec, s[2:3]
	s_waitcnt lgkmcnt(0)
	v_add_u32_e32 v112, v151, v150
	ds_read_b128 v[100:103], v112 offset:224
	ds_read_b128 v[104:107], v112 offset:192
	ds_read_b128 v[108:111], v112 offset:160
	ds_read_b128 v[112:115], v112 offset:128
	s_waitcnt lgkmcnt(3)
	v_pk_mul_f32 v[60:61], v[60:61], v[100:101]
	s_waitcnt lgkmcnt(2)
	v_pk_mul_f32 v[56:57], v[56:57], v[104:105]
	s_waitcnt lgkmcnt(1)
	v_pk_mul_f32 v[52:53], v[52:53], v[108:109]
	v_pk_mul_f32 v[62:63], v[62:63], v[102:103]
	v_pk_mul_f32 v[58:59], v[58:59], v[106:107]
	v_pk_mul_f32 v[54:55], v[54:55], v[110:111]
	s_waitcnt lgkmcnt(0)
	v_pk_mul_f32 v[50:51], v[50:51], v[114:115]
	v_pk_mul_f32 v[48:49], v[48:49], v[112:113]
	v_pk_mul_f32 v[44:45], v[44:45], v[100:101]
	v_pk_mul_f32 v[40:41], v[40:41], v[104:105]
	v_pk_mul_f32 v[36:37], v[36:37], v[108:109]
	v_pk_mul_f32 v[46:47], v[46:47], v[102:103]
	v_pk_mul_f32 v[42:43], v[42:43], v[106:107]
	v_pk_mul_f32 v[38:39], v[38:39], v[110:111]
	v_pk_mul_f32 v[34:35], v[34:35], v[114:115]
	v_pk_mul_f32 v[32:33], v[32:33], v[112:113]
	v_pk_mul_f32 v[28:29], v[28:29], v[100:101]
	v_pk_mul_f32 v[24:25], v[24:25], v[104:105]
	v_pk_mul_f32 v[20:21], v[20:21], v[108:109]
	v_pk_mul_f32 v[30:31], v[30:31], v[102:103]
	v_pk_mul_f32 v[26:27], v[26:27], v[106:107]
	v_pk_mul_f32 v[22:23], v[22:23], v[110:111]
	v_pk_mul_f32 v[18:19], v[18:19], v[114:115]
	v_pk_mul_f32 v[16:17], v[16:17], v[112:113]
	v_pk_mul_f32 v[12:13], v[12:13], v[100:101]
	v_pk_mul_f32 v[8:9], v[8:9], v[104:105]
	v_pk_mul_f32 v[4:5], v[4:5], v[108:109]
	v_pk_mul_f32 v[14:15], v[14:15], v[102:103]
	v_pk_mul_f32 v[10:11], v[10:11], v[106:107]
	v_pk_mul_f32 v[6:7], v[6:7], v[110:111]
	v_pk_mul_f32 v[2:3], v[2:3], v[114:115]
	v_pk_mul_f32 v[0:1], v[0:1], v[112:113]
